# NORM2: per-batch modulation vectors (12 loads) requested in one round trip instead of four dependent rounds
# baseline (speedup 1.0000x reference)
.LBB0_1116:
	s_lshl_b32 s20, s62, 5
	s_add_i32 s20, s20, s13
	s_add_i32 s0, s20, 0xffffe000
	s_ashr_i32 s0, s0, 11
	s_cmpk_gt_i32 s20, 0x1fff
	s_cselect_b32 s48, s0, 32
	s_cmp_eq_u32 s48, s83
	s_cbranch_scc1 .LBB0_1118
	s_ashr_i32 s0, s48, 31
	s_mul_i32 s1, s24, 33
	s_add_u32 s1, s1, s48
	s_mul_hi_u32 s14, s24, 33
	s_addc_u32 s0, s14, s0
	s_mulk_i32 s0, 0x6000
	s_mul_hi_u32 s14, s1, 0x6000
	s_add_i32 s14, s14, s0
	s_mulk_i32 s1, 0x6000
	s_add_u32 s15, s64, s1
	s_load_dwordx2 s[0:1], s[28:29], 0x38
	s_addc_u32 s49, s65, s14
	s_mov_b32 s83, s48
	s_waitcnt lgkmcnt(0)
	s_add_u32 s46, s0, s56
	s_addc_u32 s47, s1, s57
	s_add_u32 s0, s15, 0x4000
	s_addc_u32 s1, s49, 0
	global_load_dwordx4 v[56:59], v87, s[0:1]
	global_load_dwordx4 v[64:67], v184, s[0:1]
	global_load_dwordx4 v[72:75], v185, s[0:1]
	global_load_dwordx4 v[76:79], v186, s[0:1]
	global_load_dwordx4 v[158:161], v87, s[46:47]
	global_load_dwordx4 v[162:165], v87, s[46:47] offset:1024
	global_load_dwordx4 v[166:169], v87, s[46:47] offset:2048
	global_load_dwordx4 v[170:173], v87, s[46:47] offset:3072
	s_add_u32 s14, s15, 0x3000
	s_addc_u32 s15, s49, 0
	global_load_dwordx4 v[52:55], v87, s[14:15]
	global_load_dwordx4 v[60:63], v184, s[14:15]
	global_load_dwordx4 v[68:71], v185, s[14:15]
	global_load_dwordx4 v[80:83], v186, s[14:15]
	s_waitcnt vmcnt(4)
	v_pk_add_f32 v[58:59], v[58:59], 1.0 op_sel_hi:[1,0]
	v_pk_add_f32 v[56:57], v[56:57], 1.0 op_sel_hi:[1,0]
	v_pk_add_f32 v[66:67], v[66:67], 1.0 op_sel_hi:[1,0]
	v_pk_add_f32 v[64:65], v[64:65], 1.0 op_sel_hi:[1,0]
	v_pk_add_f32 v[74:75], v[74:75], 1.0 op_sel_hi:[1,0]
	v_pk_add_f32 v[72:73], v[72:73], 1.0 op_sel_hi:[1,0]
	v_pk_add_f32 v[78:79], v[78:79], 1.0 op_sel_hi:[1,0]
	v_pk_add_f32 v[76:77], v[76:77], 1.0 op_sel_hi:[1,0]
	v_pk_mul_f32 v[58:59], v[160:161], v[58:59]
	v_pk_mul_f32 v[56:57], v[158:159], v[56:57]
	v_pk_mul_f32 v[66:67], v[164:165], v[66:67]
	v_pk_mul_f32 v[64:65], v[162:163], v[64:65]
	v_pk_mul_f32 v[74:75], v[168:169], v[74:75]
	v_pk_mul_f32 v[72:73], v[166:167], v[72:73]
	v_pk_mul_f32 v[78:79], v[172:173], v[78:79]
	v_pk_mul_f32 v[76:77], v[170:171], v[76:77]
